# gMLP unit: the four staging loads of each channel group issued together at the top of the group (were four serialized load+vmcnt(0) round trips), counted waits
# speedup vs baseline: 1.0063x; 1.0004x over previous
; #define LAS __attribute__((address_space(3)))
; __device__ __forceinline__ float bflo(unsigned w) { return __uint_as_float(w << 16); }
; __device__ __forceinline__ float bfhi(unsigned w) { return __uint_as_float(w & 0xffff0000u); }
; __device__ __forceinline__ float gelu_fast(float x) { const float y = 1.5957691216057308f * (x + 0.044715f * x * x * x); return x * __builtin_amdgcn_rcpf(1.f + __expf(-y)); }
; __device__ __forceinline__ void gmlp_fast_unit(int ci, const bf16_t* P, const float* gnorm, const bf16_t* Wb, const float* bs_, bf16_t* AO, LAS unsigned char* lds) {
;     ...
;     for (int g = 0; g < 8; ++g) {
; #pragma unroll
;         for (int i = 0; i < 4; ++i) { const int id = tid + 512 * i, s = id >> 4, ch = id & 15;
;             const u32x4 w = *(const u32x4*)(P + (size_t)(row0 + s) * LDP0 + 3072 + g * 128 + 8 * ch); const unsigned ww[4] = {w.x, w.y, w.z, w.w};
;             const float rr = rs[s]; const f32x4 g0 = *(const LAS f32x4*)(gnl + g * 128 + 8 * ch), g1 = *(const LAS f32x4*)(gnl + g * 128 + 8 * ch + 4);
;             const float gg[8] = {g0[0], g0[1], g0[2], g0[3], g1[0], g1[1], g1[2], g1[3]};
;             unsigned ow[4];
; #pragma unroll
;             for (int c = 0; c < 4; ++c) ow[c] = pk2(gelu_fast(bflo(ww[c])) * rr * gg[2 * c], gelu_fast(bfhi(ww[c])) * rr * gg[2 * c + 1]);
;             *(LAS u32x4*)(lds + GM_VT + s * GM_RS + ch * 16) = (u32x4){ow[0], ow[1], ow[2], ow[3]}; }
.LBB0_293:
	v_lshl_add_u64 v[2:3], s[94:95], 0, v[38:39]
	global_load_dwordx4 v[10:13], v[2:3], off
	v_lshl_add_u64 v[104:105], s[94:95], 0, v[40:41]
	global_load_dwordx4 v[104:107], v[104:105], off
	v_lshl_add_u64 v[108:109], s[94:95], 0, v[42:43]
	global_load_dwordx4 v[108:111], v[108:109], off
	v_lshl_add_u64 v[112:113], s[94:95], 0, v[44:45]
	global_load_dwordx4 v[112:115], v[112:113], off
	v_add_u32_e32 v4, s2, v184
	ds_read_b32 v14, v179 offset:36864
	ds_read_b128 v[6:9], v4
	ds_read_b128 v[2:5], v4 offset:16
	s_mov_b32 s3, 0x280000
	v_add_u32_e32 v64, s2, v65
	s_addk_i32 s2, 0x200
	s_mov_b64 s[8:9], 0x8000
	v_lshl_add_u64 v[38:39], v[38:39], 0, s[20:21]
	s_cmpk_eq_i32 s2, 0x1000
	s_waitcnt vmcnt(3)
	v_lshlrev_b32_e32 v16, 16, v10
	v_and_b32_e32 v17, 0xffff0000, v10
	v_mul_f32_e32 v10, 0x3d372713, v16
	v_mul_f32_e32 v10, v10, v16
	v_mov_b32_e32 v15, v16
	v_fmac_f32_e32 v15, v10, v15
	v_mul_f32_e32 v10, 0xbfcc422a, v15
	v_mul_f32_e32 v10, 0x3fb8aa3b, v10
	v_exp_f32_e32 v10, v10
	v_mov_b32_e32 v15, v17
	v_add_f32_e32 v10, 1.0, v10
	v_rcp_f32_e32 v18, v10
	v_mul_f32_e32 v10, 0x3d372713, v17
	v_mul_f32_e32 v10, v10, v17
	v_fmac_f32_e32 v15, v10, v15
	v_mul_f32_e32 v10, 0xbfcc422a, v15
	v_mul_f32_e32 v10, 0x3fb8aa3b, v10
	v_exp_f32_e32 v10, v10
	s_nop 0
	v_add_f32_e32 v10, 1.0, v10
	v_rcp_f32_e32 v19, v10
	s_nop 0
	v_pk_mul_f32 v[16:17], v[18:19], v[16:17]
	s_waitcnt lgkmcnt(2)
	v_pk_mul_f32 v[16:17], v[14:15], v[16:17] op_sel_hi:[0,1]
	s_waitcnt lgkmcnt(1)
	v_pk_mul_f32 v[16:17], v[6:7], v[16:17]
	s_nop 0
	v_cvt_pk_bf16_f32 v10, v16, v17
	v_lshlrev_b32_e32 v16, 16, v11
	v_and_b32_e32 v17, 0xffff0000, v11
	v_mul_f32_e32 v11, 0x3d372713, v16
	v_mul_f32_e32 v11, v11, v16
	v_mov_b32_e32 v15, v16
	v_fmac_f32_e32 v15, v11, v15
	v_mul_f32_e32 v11, 0xbfcc422a, v15
	v_mul_f32_e32 v11, 0x3fb8aa3b, v11
	v_exp_f32_e32 v11, v11
	v_mov_b32_e32 v15, v17
	v_add_f32_e32 v11, 1.0, v11
	v_rcp_f32_e32 v18, v11
	v_mul_f32_e32 v11, 0x3d372713, v17
	v_mul_f32_e32 v11, v11, v17
	v_fmac_f32_e32 v15, v11, v15
	v_mul_f32_e32 v11, 0xbfcc422a, v15
	v_mul_f32_e32 v11, 0x3fb8aa3b, v11
	v_exp_f32_e32 v11, v11
	s_nop 0
	v_add_f32_e32 v11, 1.0, v11
	v_rcp_f32_e32 v19, v11
	s_nop 0
	v_pk_mul_f32 v[16:17], v[18:19], v[16:17]
	s_nop 0
	v_pk_mul_f32 v[16:17], v[14:15], v[16:17] op_sel_hi:[0,1]
	v_pk_mul_f32 v[16:17], v[8:9], v[16:17]
	s_nop 0
	v_cvt_pk_bf16_f32 v11, v16, v17
	v_lshlrev_b32_e32 v16, 16, v12
	v_and_b32_e32 v17, 0xffff0000, v12
	v_mul_f32_e32 v12, 0x3d372713, v16
	v_mul_f32_e32 v12, v12, v16
	v_mov_b32_e32 v15, v16
	v_fmac_f32_e32 v15, v12, v15
	v_mul_f32_e32 v12, 0xbfcc422a, v15
	v_mul_f32_e32 v12, 0x3fb8aa3b, v12
	v_exp_f32_e32 v12, v12
	v_mov_b32_e32 v15, v17
	v_add_f32_e32 v12, 1.0, v12
	v_rcp_f32_e32 v18, v12
	v_mul_f32_e32 v12, 0x3d372713, v17
	v_mul_f32_e32 v12, v12, v17
	v_fmac_f32_e32 v15, v12, v15
	v_mul_f32_e32 v12, 0xbfcc422a, v15
	v_mul_f32_e32 v12, 0x3fb8aa3b, v12
	v_exp_f32_e32 v12, v12
	s_nop 0
	v_add_f32_e32 v12, 1.0, v12
	v_rcp_f32_e32 v19, v12
	s_nop 0
	v_pk_mul_f32 v[16:17], v[18:19], v[16:17]
	s_nop 0
	v_pk_mul_f32 v[16:17], v[14:15], v[16:17] op_sel_hi:[0,1]
	s_waitcnt lgkmcnt(0)
	v_pk_mul_f32 v[16:17], v[2:3], v[16:17]
	s_nop 0
	v_cvt_pk_bf16_f32 v12, v16, v17
	v_lshlrev_b32_e32 v16, 16, v13
	v_and_b32_e32 v17, 0xffff0000, v13
	v_mul_f32_e32 v13, 0x3d372713, v16
	v_mul_f32_e32 v13, v13, v16
	v_mov_b32_e32 v15, v16
	v_fmac_f32_e32 v15, v13, v15
	v_mul_f32_e32 v13, 0xbfcc422a, v15
	v_mul_f32_e32 v13, 0x3fb8aa3b, v13
	v_exp_f32_e32 v13, v13
	v_mov_b32_e32 v15, v17
	v_add_f32_e32 v13, 1.0, v13
	v_rcp_f32_e32 v18, v13
	v_mul_f32_e32 v13, 0x3d372713, v17
	v_mul_f32_e32 v13, v13, v17
	v_fmac_f32_e32 v15, v13, v15
	v_mul_f32_e32 v13, 0xbfcc422a, v15
	v_mul_f32_e32 v13, 0x3fb8aa3b, v13
	v_exp_f32_e32 v13, v13
	s_nop 0
	v_add_f32_e32 v13, 1.0, v13
	v_rcp_f32_e32 v19, v13
	s_nop 0
	v_pk_mul_f32 v[16:17], v[18:19], v[16:17]
	s_nop 0
	v_pk_mul_f32 v[14:15], v[14:15], v[16:17] op_sel_hi:[0,1]
	v_pk_mul_f32 v[14:15], v[4:5], v[14:15]
	s_nop 0
	v_cvt_pk_bf16_f32 v13, v14, v15
	v_add_u32_e32 v14, v178, v152
	ds_write_b128 v14, v[10:13]
	ds_read_b32 v16, v180 offset:36864
	v_lshl_add_u64 v[40:41], v[40:41], 0, s[20:21]
	s_waitcnt vmcnt(2)
	v_mov_b32_e32 v10, v104
	v_mov_b32_e32 v11, v105
	v_mov_b32_e32 v12, v106
	v_mov_b32_e32 v13, v107
	v_lshlrev_b32_e32 v18, 16, v10
	v_and_b32_e32 v19, 0xffff0000, v10
	v_mul_f32_e32 v10, 0x3d372713, v18
	v_mul_f32_e32 v10, v10, v18
	v_mov_b32_e32 v15, v18
	v_fmac_f32_e32 v15, v10, v15
	v_mul_f32_e32 v10, 0xbfcc422a, v15
	v_mul_f32_e32 v10, 0x3fb8aa3b, v10
	v_exp_f32_e32 v10, v10
	v_mov_b32_e32 v15, v19
	v_add_f32_e32 v10, 1.0, v10
	v_rcp_f32_e32 v20, v10
	v_mul_f32_e32 v10, 0x3d372713, v19
	v_mul_f32_e32 v10, v10, v19
	v_fmac_f32_e32 v15, v10, v15
	v_mul_f32_e32 v10, 0xbfcc422a, v15
	v_mul_f32_e32 v10, 0x3fb8aa3b, v10
	v_exp_f32_e32 v10, v10
	s_nop 0
	v_add_f32_e32 v10, 1.0, v10
	v_rcp_f32_e32 v21, v10
	s_nop 0
	v_pk_mul_f32 v[18:19], v[20:21], v[18:19]
	s_waitcnt lgkmcnt(0)
; #define LAS __attribute__((address_space(3)))
; __device__ __forceinline__ float bflo(unsigned w) { return __uint_as_float(w << 16); }
; __device__ __forceinline__ float bfhi(unsigned w) { return __uint_as_float(w & 0xffff0000u); }
; __device__ __forceinline__ float gelu_fast(float x) { const float y = 1.5957691216057308f * (x + 0.044715f * x * x * x); return x * __builtin_amdgcn_rcpf(1.f + __expf(-y)); }
; __device__ __forceinline__ void gmlp_fast_unit(int ci, const bf16_t* P, const float* gnorm, const bf16_t* Wb, const float* bs_, bf16_t* AO, LAS unsigned char* lds) {
;     ...
;         for (int i = 0; i < 4; ++i) { const int id = tid + 512 * i, s = id >> 4, ch = id & 15;
;             const u32x4 w = *(const u32x4*)(P + (size_t)(row0 + s) * LDP0 + 3072 + g * 128 + 8 * ch); const unsigned ww[4] = {w.x, w.y, w.z, w.w};
;             const float rr = rs[s]; const f32x4 g0 = *(const LAS f32x4*)(gnl + g * 128 + 8 * ch), g1 = *(const LAS f32x4*)(gnl + g * 128 + 8 * ch + 4);
;             const float gg[8] = {g0[0], g0[1], g0[2], g0[3], g1[0], g1[1], g1[2], g1[3]};
;             unsigned ow[4];
; #pragma unroll
;             for (int c = 0; c < 4; ++c) ow[c] = pk2(gelu_fast(bflo(ww[c])) * rr * gg[2 * c], gelu_fast(bfhi(ww[c])) * rr * gg[2 * c + 1]);
;             *(LAS u32x4*)(lds + GM_VT + s * GM_RS + ch * 16) = (u32x4){ow[0], ow[1], ow[2], ow[3]}; }
	v_pk_mul_f32 v[18:19], v[16:17], v[18:19] op_sel_hi:[0,1]
	v_pk_mul_f32 v[18:19], v[6:7], v[18:19]
	s_nop 0
	v_cvt_pk_bf16_f32 v10, v18, v19
	v_lshlrev_b32_e32 v18, 16, v11
	v_and_b32_e32 v19, 0xffff0000, v11
	v_mul_f32_e32 v11, 0x3d372713, v18
	v_mul_f32_e32 v11, v11, v18
	v_mov_b32_e32 v15, v18
	v_fmac_f32_e32 v15, v11, v15
	v_mul_f32_e32 v11, 0xbfcc422a, v15
	v_mul_f32_e32 v11, 0x3fb8aa3b, v11
	v_exp_f32_e32 v11, v11
	v_mov_b32_e32 v15, v19
	v_add_f32_e32 v11, 1.0, v11
	v_rcp_f32_e32 v20, v11
	v_mul_f32_e32 v11, 0x3d372713, v19
	v_mul_f32_e32 v11, v11, v19
	v_fmac_f32_e32 v15, v11, v15
	v_mul_f32_e32 v11, 0xbfcc422a, v15
	v_mul_f32_e32 v11, 0x3fb8aa3b, v11
	v_exp_f32_e32 v11, v11
	s_nop 0
	v_add_f32_e32 v11, 1.0, v11
	v_rcp_f32_e32 v21, v11
	s_nop 0
	v_pk_mul_f32 v[18:19], v[20:21], v[18:19]
	s_nop 0
	v_pk_mul_f32 v[18:19], v[16:17], v[18:19] op_sel_hi:[0,1]
	v_pk_mul_f32 v[18:19], v[8:9], v[18:19]
	s_nop 0
	v_cvt_pk_bf16_f32 v11, v18, v19
	v_lshlrev_b32_e32 v18, 16, v12
	v_and_b32_e32 v19, 0xffff0000, v12
	v_mul_f32_e32 v12, 0x3d372713, v18
	v_mul_f32_e32 v12, v12, v18
	v_mov_b32_e32 v15, v18
	v_fmac_f32_e32 v15, v12, v15
	v_mul_f32_e32 v12, 0xbfcc422a, v15
	v_mul_f32_e32 v12, 0x3fb8aa3b, v12
	v_exp_f32_e32 v12, v12
	v_mov_b32_e32 v15, v19
	v_add_f32_e32 v12, 1.0, v12
	v_rcp_f32_e32 v20, v12
	v_mul_f32_e32 v12, 0x3d372713, v19
	v_mul_f32_e32 v12, v12, v19
	v_fmac_f32_e32 v15, v12, v15
	v_mul_f32_e32 v12, 0xbfcc422a, v15
	v_mul_f32_e32 v12, 0x3fb8aa3b, v12
	v_exp_f32_e32 v12, v12
	s_nop 0
	v_add_f32_e32 v12, 1.0, v12
	v_rcp_f32_e32 v21, v12
	s_nop 0
	v_pk_mul_f32 v[18:19], v[20:21], v[18:19]
	s_nop 0
	v_pk_mul_f32 v[18:19], v[16:17], v[18:19] op_sel_hi:[0,1]
	v_pk_mul_f32 v[18:19], v[2:3], v[18:19]
	s_nop 0
	v_cvt_pk_bf16_f32 v12, v18, v19
	v_lshlrev_b32_e32 v18, 16, v13
	v_and_b32_e32 v19, 0xffff0000, v13
	v_mul_f32_e32 v13, 0x3d372713, v18
	v_mul_f32_e32 v13, v13, v18
	v_mov_b32_e32 v15, v18
	v_fmac_f32_e32 v15, v13, v15
	v_mul_f32_e32 v13, 0xbfcc422a, v15
	v_mul_f32_e32 v13, 0x3fb8aa3b, v13
	v_exp_f32_e32 v13, v13
	v_mov_b32_e32 v15, v19
	v_add_f32_e32 v13, 1.0, v13
	v_rcp_f32_e32 v20, v13
	v_mul_f32_e32 v13, 0x3d372713, v19
	v_mul_f32_e32 v13, v13, v19
	v_fmac_f32_e32 v15, v13, v15
	v_mul_f32_e32 v13, 0xbfcc422a, v15
	v_mul_f32_e32 v13, 0x3fb8aa3b, v13
	v_exp_f32_e32 v13, v13
	v_add_u32_e32 v15, v178, v156
	v_add_f32_e32 v13, 1.0, v13
	v_rcp_f32_e32 v21, v13
	s_nop 0
	v_pk_mul_f32 v[18:19], v[20:21], v[18:19]
	s_nop 0
	v_pk_mul_f32 v[16:17], v[16:17], v[18:19] op_sel_hi:[0,1]
	v_pk_mul_f32 v[16:17], v[4:5], v[16:17]
	s_nop 0
	v_cvt_pk_bf16_f32 v13, v16, v17
	ds_write_b128 v15, v[10:13]
	ds_read_b32 v16, v179 offset:37120
	v_lshl_add_u64 v[42:43], v[42:43], 0, s[20:21]
	s_waitcnt vmcnt(1)
	v_mov_b32_e32 v10, v108
	v_mov_b32_e32 v11, v109
	v_mov_b32_e32 v12, v110
	v_mov_b32_e32 v13, v111
	v_lshlrev_b32_e32 v18, 16, v10
	v_and_b32_e32 v19, 0xffff0000, v10
	v_mul_f32_e32 v10, 0x3d372713, v18
	v_mul_f32_e32 v10, v10, v18
	v_mov_b32_e32 v15, v18
	v_fmac_f32_e32 v15, v10, v15
	v_mul_f32_e32 v10, 0xbfcc422a, v15
	v_mul_f32_e32 v10, 0x3fb8aa3b, v10
	v_exp_f32_e32 v10, v10
	v_mov_b32_e32 v15, v19
	v_add_f32_e32 v10, 1.0, v10
	v_rcp_f32_e32 v20, v10
	v_mul_f32_e32 v10, 0x3d372713, v19
	v_mul_f32_e32 v10, v10, v19
	v_fmac_f32_e32 v15, v10, v15
	v_mul_f32_e32 v10, 0xbfcc422a, v15
	v_mul_f32_e32 v10, 0x3fb8aa3b, v10
	v_exp_f32_e32 v10, v10
	s_nop 0
	v_add_f32_e32 v10, 1.0, v10
	v_rcp_f32_e32 v21, v10
	s_nop 0
	v_pk_mul_f32 v[18:19], v[20:21], v[18:19]
	s_waitcnt lgkmcnt(0)
	v_pk_mul_f32 v[18:19], v[16:17], v[18:19] op_sel_hi:[0,1]
	v_pk_mul_f32 v[18:19], v[6:7], v[18:19]
	s_nop 0
	v_cvt_pk_bf16_f32 v10, v18, v19
	v_lshlrev_b32_e32 v18, 16, v11
	v_and_b32_e32 v19, 0xffff0000, v11
	v_mul_f32_e32 v11, 0x3d372713, v18
	v_mul_f32_e32 v11, v11, v18
	v_mov_b32_e32 v15, v18
	v_fmac_f32_e32 v15, v11, v15
	v_mul_f32_e32 v11, 0xbfcc422a, v15
	v_mul_f32_e32 v11, 0x3fb8aa3b, v11
	v_exp_f32_e32 v11, v11
	v_mov_b32_e32 v15, v19
	v_add_f32_e32 v11, 1.0, v11
	v_rcp_f32_e32 v20, v11
	v_mul_f32_e32 v11, 0x3d372713, v19
	v_mul_f32_e32 v11, v11, v19
	v_fmac_f32_e32 v15, v11, v15
	v_mul_f32_e32 v11, 0xbfcc422a, v15
	v_mul_f32_e32 v11, 0x3fb8aa3b, v11
	v_exp_f32_e32 v11, v11
	s_nop 0
	v_add_f32_e32 v11, 1.0, v11
	v_rcp_f32_e32 v21, v11
	s_nop 0
	v_pk_mul_f32 v[18:19], v[20:21], v[18:19]
	s_nop 0
	v_pk_mul_f32 v[18:19], v[16:17], v[18:19] op_sel_hi:[0,1]
	v_pk_mul_f32 v[18:19], v[8:9], v[18:19]
	s_nop 0
	v_cvt_pk_bf16_f32 v11, v18, v19
	v_lshlrev_b32_e32 v18, 16, v12
	v_and_b32_e32 v19, 0xffff0000, v12
	v_mul_f32_e32 v12, 0x3d372713, v18
	v_mul_f32_e32 v12, v12, v18
	v_mov_b32_e32 v15, v18
	v_fmac_f32_e32 v15, v12, v15
	v_mul_f32_e32 v12, 0xbfcc422a, v15
	v_mul_f32_e32 v12, 0x3fb8aa3b, v12
	v_exp_f32_e32 v12, v12
	v_mov_b32_e32 v15, v19
	v_add_f32_e32 v12, 1.0, v12
	v_rcp_f32_e32 v20, v12
	v_mul_f32_e32 v12, 0x3d372713, v19
	v_mul_f32_e32 v12, v12, v19
	v_fmac_f32_e32 v15, v12, v15
	v_mul_f32_e32 v12, 0xbfcc422a, v15
	v_mul_f32_e32 v12, 0x3fb8aa3b, v12
	v_exp_f32_e32 v12, v12
	s_nop 0
	v_add_f32_e32 v12, 1.0, v12
	v_rcp_f32_e32 v21, v12
	s_nop 0
	v_pk_mul_f32 v[18:19], v[20:21], v[18:19]
	s_nop 0
	v_pk_mul_f32 v[18:19], v[16:17], v[18:19] op_sel_hi:[0,1]
	v_pk_mul_f32 v[18:19], v[2:3], v[18:19]
	s_nop 0
	v_cvt_pk_bf16_f32 v12, v18, v19
	v_lshlrev_b32_e32 v18, 16, v13
	v_and_b32_e32 v19, 0xffff0000, v13
	v_mul_f32_e32 v13, 0x3d372713, v18
	v_mul_f32_e32 v13, v13, v18
	v_mov_b32_e32 v15, v18
	v_fmac_f32_e32 v15, v13, v15
	v_mul_f32_e32 v13, 0xbfcc422a, v15
	v_mul_f32_e32 v13, 0x3fb8aa3b, v13
	v_exp_f32_e32 v13, v13
	v_mov_b32_e32 v15, v19
	v_add_f32_e32 v13, 1.0, v13
	v_rcp_f32_e32 v20, v13
	v_mul_f32_e32 v13, 0x3d372713, v19
	v_mul_f32_e32 v13, v13, v19
	v_fmac_f32_e32 v15, v13, v15
	v_mul_f32_e32 v13, 0xbfcc422a, v15
	v_mul_f32_e32 v13, 0x3fb8aa3b, v13
	v_exp_f32_e32 v13, v13
	s_nop 0
	v_add_f32_e32 v13, 1.0, v13
	v_rcp_f32_e32 v21, v13
	s_nop 0
	v_pk_mul_f32 v[18:19], v[20:21], v[18:19]
	s_nop 0
	v_pk_mul_f32 v[16:17], v[16:17], v[18:19] op_sel_hi:[0,1]
	v_pk_mul_f32 v[16:17], v[4:5], v[16:17]
	s_nop 0
	v_cvt_pk_bf16_f32 v13, v16, v17
	ds_write_b128 v14, v[10:13] offset:18432
	ds_read_b32 v14, v181 offset:36864
	v_lshl_add_u64 v[44:45], v[44:45], 0, s[20:21]
	s_waitcnt vmcnt(0)
; #define LAS __attribute__((address_space(3)))
; __device__ __forceinline__ float bflo(unsigned w) { return __uint_as_float(w << 16); }
; __device__ __forceinline__ float bfhi(unsigned w) { return __uint_as_float(w & 0xffff0000u); }
; __device__ __forceinline__ void lds_barrier() { asm volatile("s_waitcnt lgkmcnt(0)" ::: "memory"); __builtin_amdgcn_s_barrier(); asm volatile("" ::: "memory"); }
; __device__ __forceinline__ float gelu_fast(float x) { const float y = 1.5957691216057308f * (x + 0.044715f * x * x * x); return x * __builtin_amdgcn_rcpf(1.f + __expf(-y)); }
; __device__ __forceinline__ void gmlp_fast_unit(int ci, const bf16_t* P, const float* gnorm, const bf16_t* Wb, const float* bs_, bf16_t* AO, LAS unsigned char* lds) {
;     ...
;         for (int i = 0; i < 4; ++i) { const int id = tid + 512 * i, s = id >> 4, ch = id & 15;
;             const u32x4 w = *(const u32x4*)(P + (size_t)(row0 + s) * LDP0 + 3072 + g * 128 + 8 * ch); const unsigned ww[4] = {w.x, w.y, w.z, w.w};
;             const float rr = rs[s]; const f32x4 g0 = *(const LAS f32x4*)(gnl + g * 128 + 8 * ch), g1 = *(const LAS f32x4*)(gnl + g * 128 + 8 * ch + 4);
;             const float gg[8] = {g0[0], g0[1], g0[2], g0[3], g1[0], g1[1], g1[2], g1[3]};
;             unsigned ow[4];
; #pragma unroll
;             for (int c = 0; c < 4; ++c) ow[c] = pk2(gelu_fast(bflo(ww[c])) * rr * gg[2 * c], gelu_fast(bfhi(ww[c])) * rr * gg[2 * c + 1]);
;             *(LAS u32x4*)(lds + GM_VT + s * GM_RS + ch * 16) = (u32x4){ow[0], ow[1], ow[2], ow[3]}; }
;         bf16x8 wf[4];
;         { const bf16_t* wp = Wb + (size_t)g * 16384 + (size_t)p * 128 + 8 * q;
; #pragma unroll
;             for (int kk = 0; kk < 4; ++kk) wf[kk] = *(const bf16x8*)(wp + 32 * kk); }
;         u32x2 uwv[8];
;         { const bf16_t* up_ = P + (size_t)(row0 + p) * LDP0 + 2048 + g * 128 + 4 * q;
; #pragma unroll
;             for (int ct = 0; ct < 8; ++ct) uwv[ct] = *(const u32x2*)(up_ + 16 * ct); }
;         lds_barrier();
	v_mov_b32_e32 v10, v112
	v_mov_b32_e32 v11, v113
	v_mov_b32_e32 v12, v114
	v_mov_b32_e32 v13, v115
	v_lshlrev_b32_e32 v16, 16, v10
	v_and_b32_e32 v17, 0xffff0000, v10
	v_mul_f32_e32 v10, 0x3d372713, v16
	v_mul_f32_e32 v10, v10, v16
	v_mov_b32_e32 v15, v16
	v_fmac_f32_e32 v15, v10, v15
	v_mul_f32_e32 v10, 0xbfcc422a, v15
	v_mul_f32_e32 v10, 0x3fb8aa3b, v10
	v_exp_f32_e32 v10, v10
	v_mov_b32_e32 v15, v17
	v_add_f32_e32 v10, 1.0, v10
	v_rcp_f32_e32 v18, v10
	v_mul_f32_e32 v10, 0x3d372713, v17
	v_mul_f32_e32 v10, v10, v17
	v_fmac_f32_e32 v15, v10, v15
	v_mul_f32_e32 v10, 0xbfcc422a, v15
	v_mul_f32_e32 v10, 0x3fb8aa3b, v10
	v_exp_f32_e32 v10, v10
	s_nop 0
	v_add_f32_e32 v10, 1.0, v10
	v_rcp_f32_e32 v19, v10
	v_lshlrev_b32_e32 v10, 16, v11
	v_and_b32_e32 v11, 0xffff0000, v11
	v_pk_mul_f32 v[16:17], v[18:19], v[16:17]
	s_waitcnt lgkmcnt(0)
	v_pk_mul_f32 v[16:17], v[14:15], v[16:17] op_sel_hi:[0,1]
	v_pk_mul_f32 v[6:7], v[6:7], v[16:17]
	v_mov_b32_e32 v15, v10
	v_cvt_pk_bf16_f32 v6, v6, v7
	v_mul_f32_e32 v7, 0x3d372713, v10
	v_mul_f32_e32 v7, v7, v10
	v_fmac_f32_e32 v15, v7, v15
	v_mul_f32_e32 v7, 0xbfcc422a, v15
	v_mul_f32_e32 v7, 0x3fb8aa3b, v7
	v_exp_f32_e32 v7, v7
	v_mov_b32_e32 v15, v11
	v_add_f32_e32 v7, 1.0, v7
	v_rcp_f32_e32 v16, v7
	v_mul_f32_e32 v7, 0x3d372713, v11
	v_mul_f32_e32 v7, v7, v11
	v_fmac_f32_e32 v15, v7, v15
	v_mul_f32_e32 v7, 0xbfcc422a, v15
	v_mul_f32_e32 v7, 0x3fb8aa3b, v7
	v_exp_f32_e32 v7, v7
	s_nop 0
	v_add_f32_e32 v7, 1.0, v7
	v_rcp_f32_e32 v17, v7
	s_nop 0
	v_pk_mul_f32 v[10:11], v[16:17], v[10:11]
	s_nop 0
	v_pk_mul_f32 v[10:11], v[14:15], v[10:11] op_sel_hi:[0,1]
	v_pk_mul_f32 v[8:9], v[8:9], v[10:11]
	s_nop 0
	v_cvt_pk_bf16_f32 v7, v8, v9
	v_lshlrev_b32_e32 v8, 16, v12
	v_mul_f32_e32 v10, 0x3d372713, v8
	v_mul_f32_e32 v10, v10, v8
	v_mov_b32_e32 v11, v8
	v_and_b32_e32 v9, 0xffff0000, v12
	v_fmac_f32_e32 v11, v10, v11
	v_mul_f32_e32 v10, 0xbfcc422a, v11
	v_mul_f32_e32 v11, 0x3d372713, v9
	v_mul_f32_e32 v11, v11, v9
	v_mov_b32_e32 v12, v9
	v_fmac_f32_e32 v12, v11, v12
	v_mul_f32_e32 v11, 0xbfcc422a, v12
	v_mul_f32_e32 v10, 0x3fb8aa3b, v10
	v_mul_f32_e32 v11, 0x3fb8aa3b, v11
	v_exp_f32_e32 v10, v10
	v_exp_f32_e32 v11, v11
	v_add_f32_e32 v10, 1.0, v10
	v_add_f32_e32 v11, 1.0, v11
	v_rcp_f32_e32 v10, v10
	v_rcp_f32_e32 v11, v11
	s_nop 0
	v_pk_mul_f32 v[8:9], v[10:11], v[8:9]
	s_nop 0
	v_pk_mul_f32 v[8:9], v[14:15], v[8:9] op_sel_hi:[0,1]
	v_pk_mul_f32 v[2:3], v[2:3], v[8:9]
	s_nop 0
	v_cvt_pk_bf16_f32 v8, v2, v3
	v_lshlrev_b32_e32 v2, 16, v13
	v_mul_f32_e32 v9, 0x3d372713, v2
	v_mul_f32_e32 v9, v9, v2
	v_mov_b32_e32 v10, v2
	v_fmac_f32_e32 v10, v9, v10
	v_mul_f32_e32 v9, 0xbfcc422a, v10
	v_mul_f32_e32 v9, 0x3fb8aa3b, v9
	v_exp_f32_e32 v9, v9
	v_and_b32_e32 v3, 0xffff0000, v13
	v_mov_b32_e32 v11, v3
	v_add_f32_e32 v9, 1.0, v9
	v_rcp_f32_e32 v10, v9
	v_mul_f32_e32 v9, 0x3d372713, v3
	v_mul_f32_e32 v9, v9, v3
	v_fmac_f32_e32 v11, v9, v11
	v_mul_f32_e32 v9, 0xbfcc422a, v11
	v_mul_f32_e32 v9, 0x3fb8aa3b, v9
	v_exp_f32_e32 v9, v9
	s_nop 0
	v_add_f32_e32 v9, 1.0, v9
	v_rcp_f32_e32 v11, v9
	s_nop 0
	v_pk_mul_f32 v[2:3], v[10:11], v[2:3]
	s_nop 0
	v_pk_mul_f32 v[2:3], v[14:15], v[2:3] op_sel_hi:[0,1]
	v_pk_mul_f32 v[2:3], v[4:5], v[2:3]
	s_nop 0
	v_cvt_pk_bf16_f32 v9, v2, v3
	v_add_u32_e32 v2, v178, v163
	ds_write_b128 v2, v[6:9]
	v_lshl_add_u64 v[2:3], s[94:95], 0, v[34:35]
	v_add_co_u32_e32 v14, vcc, s3, v2
	s_mov_b32 s3, 0x41e01000
	s_nop 0
	v_addc_co_u32_e32 v15, vcc, 0, v3, vcc
	global_load_dwordx4 v[2:5], v[14:15], off
	global_load_dwordx4 v[6:9], v[14:15], off offset:64
	global_load_dwordx4 v[10:13], v[14:15], off offset:128
	global_load_dwordx4 v[66:69], v[14:15], off offset:192
	v_lshl_add_u64 v[14:15], s[94:95], 0, v[46:47]
	v_add_co_u32_e32 v14, vcc, s3, v14
	s_mov_b32 s3, 0x4f300000
	s_nop 0
	v_addc_co_u32_e32 v15, vcc, 0, v15, vcc
	global_load_dwordx2 v[62:63], v[14:15], off
	global_load_dwordx2 v[60:61], v[14:15], off offset:32
	global_load_dwordx2 v[58:59], v[14:15], off offset:64
	global_load_dwordx2 v[56:57], v[14:15], off offset:96
	global_load_dwordx2 v[54:55], v[14:15], off offset:128
	global_load_dwordx2 v[52:53], v[14:15], off offset:160
	global_load_dwordx2 v[50:51], v[14:15], off offset:192
	global_load_dwordx2 v[48:49], v[14:15], off offset:224
	s_waitcnt lgkmcnt(0)
	s_barrier
; __device__ __forceinline__ void lds_barrier() { asm volatile("s_waitcnt lgkmcnt(0)" ::: "memory"); __builtin_amdgcn_s_barrier(); asm volatile("" ::: "memory"); }
; __device__ __forceinline__ void gmlp_fast_unit(int ci, const bf16_t* P, const float* gnorm, const bf16_t* Wb, const float* bs_, bf16_t* AO, LAS unsigned char* lds) {
;     ...
;         f32x4 acc[8];
; #pragma unroll
;         for (int ct = 0; ct < 8; ++ct) acc[ct] = (f32x4){0.f, 0.f, 0.f, 0.f};
; #pragma unroll
;         for (int kk = 0; kk < 4; ++kk)
; #pragma unroll
;             for (int ct = 0; ct < 8; ++ct) { const bf16x8 vf = tr_frag(lds + GM_VT + (32 * kk + 8 * q + trq) * GM_RS + (16 * ct + 4 * trp) * 2, 4 * GM_RS);
;                 acc[ct] = __builtin_amdgcn_mfma_f32_16x16x32_bf16(vf, wf[kk], acc[ct], 0, 0, 0); }
;         lds_barrier();
	ds_read_b64_tr_b16 v[16:17], v182 offset:1152
	ds_read_b64_tr_b16 v[14:15], v182
	ds_read_b64_tr_b16 v[18:19], v182 offset:32
	ds_read_b64_tr_b16 v[20:21], v182 offset:1184
	ds_read_b64_tr_b16 v[22:23], v182 offset:64
	ds_read_b64_tr_b16 v[24:25], v182 offset:1216
	ds_read_b64_tr_b16 v[26:27], v182 offset:96
	ds_read_b64_tr_b16 v[28:29], v182 offset:1248
	ds_read_b64_tr_b16 v[30:31], v182 offset:128
	ds_read_b64_tr_b16 v[32:33], v182 offset:1280
	ds_read_b64_tr_b16 v[70:71], v182 offset:160
	ds_read_b64_tr_b16 v[72:73], v182 offset:1312
	ds_read_b64_tr_b16 v[74:75], v182 offset:192
	ds_read_b64_tr_b16 v[76:77], v182 offset:1344
	ds_read_b64_tr_b16 v[78:79], v182 offset:224
	ds_read_b64_tr_b16 v[80:81], v182 offset:1376
	s_waitcnt vmcnt(11) lgkmcnt(14)
	v_mfma_f32_16x16x32_bf16 v[14:17], v[14:17], v[2:5], 0
	v_lshl_add_u64 v[34:35], v[34:35], 0, s[8:9]
	v_lshl_add_u64 v[46:47], v[46:47], 0, s[20:21]
	s_waitcnt lgkmcnt(12)
	v_mfma_f32_16x16x32_bf16 v[18:21], v[18:21], v[2:5], 0
	s_waitcnt lgkmcnt(10)
	v_mfma_f32_16x16x32_bf16 v[22:25], v[22:25], v[2:5], 0
	s_waitcnt lgkmcnt(8)
	v_mfma_f32_16x16x32_bf16 v[26:29], v[26:29], v[2:5], 0
	s_waitcnt lgkmcnt(6)
	v_mfma_f32_16x16x32_bf16 v[30:33], v[30:33], v[2:5], 0
	s_waitcnt lgkmcnt(4)
	v_mfma_f32_16x16x32_bf16 v[70:73], v[70:73], v[2:5], 0
	s_waitcnt lgkmcnt(2)
	v_mfma_f32_16x16x32_bf16 v[74:77], v[74:77], v[2:5], 0
	s_waitcnt lgkmcnt(0)
	v_mfma_f32_16x16x32_bf16 v[2:5], v[78:81], v[2:5], 0
	ds_read_b64_tr_b16 v[78:79], v182 offset:9216
	ds_read_b64_tr_b16 v[80:81], v182 offset:10368
	s_waitcnt vmcnt(10) lgkmcnt(0)
	v_mfma_f32_16x16x32_bf16 v[14:17], v[78:81], v[6:9], v[14:17]
	ds_read_b64_tr_b16 v[78:79], v182 offset:9248
	ds_read_b64_tr_b16 v[80:81], v182 offset:10400
	s_waitcnt lgkmcnt(0)
	v_mfma_f32_16x16x32_bf16 v[18:21], v[78:81], v[6:9], v[18:21]
	ds_read_b64_tr_b16 v[78:79], v182 offset:9280
	ds_read_b64_tr_b16 v[80:81], v182 offset:10432
	s_waitcnt lgkmcnt(0)
	v_mfma_f32_16x16x32_bf16 v[22:25], v[78:81], v[6:9], v[22:25]
	ds_read_b64_tr_b16 v[78:79], v182 offset:9312
	ds_read_b64_tr_b16 v[80:81], v182 offset:10464
	s_waitcnt lgkmcnt(0)
	v_mfma_f32_16x16x32_bf16 v[26:29], v[78:81], v[6:9], v[26:29]
	ds_read_b64_tr_b16 v[78:79], v182 offset:9344
	ds_read_b64_tr_b16 v[80:81], v182 offset:10496
	s_waitcnt lgkmcnt(0)
	v_mfma_f32_16x16x32_bf16 v[30:33], v[78:81], v[6:9], v[30:33]
	ds_read_b64_tr_b16 v[78:79], v182 offset:9376
	ds_read_b64_tr_b16 v[80:81], v182 offset:10528
	s_waitcnt lgkmcnt(0)
	v_mfma_f32_16x16x32_bf16 v[70:73], v[78:81], v[6:9], v[70:73]
	ds_read_b64_tr_b16 v[78:79], v182 offset:9408
	ds_read_b64_tr_b16 v[80:81], v182 offset:10560
	s_waitcnt lgkmcnt(0)
	v_mfma_f32_16x16x32_bf16 v[74:77], v[78:81], v[6:9], v[74:77]
	ds_read_b64_tr_b16 v[78:79], v182 offset:9440
	ds_read_b64_tr_b16 v[80:81], v182 offset:10592
	s_waitcnt lgkmcnt(0)
	v_mfma_f32_16x16x32_bf16 v[2:5], v[78:81], v[6:9], v[2:5]
	ds_read_b64_tr_b16 v[6:7], v182 offset:18432
	ds_read_b64_tr_b16 v[8:9], v182 offset:19584
	s_waitcnt vmcnt(9) lgkmcnt(0)
	v_mfma_f32_16x16x32_bf16 v[6:9], v[6:9], v[10:13], v[14:17]
	s_nop 2
	ds_read_b64_tr_b16 v[14:15], v182 offset:18464
	ds_read_b64_tr_b16 v[16:17], v182 offset:19616
	s_waitcnt lgkmcnt(0)
	v_mfma_f32_16x16x32_bf16 v[14:17], v[14:17], v[10:13], v[18:21]
	s_nop 2
	ds_read_b64_tr_b16 v[18:19], v182 offset:18496
	ds_read_b64_tr_b16 v[20:21], v182 offset:19648
	s_waitcnt lgkmcnt(0)
	v_mfma_f32_16x16x32_bf16 v[18:21], v[18:21], v[10:13], v[22:25]
	s_nop 2
	ds_read_b64_tr_b16 v[22:23], v182 offset:18528
	ds_read_b64_tr_b16 v[24:25], v182 offset:19680
	s_waitcnt lgkmcnt(0)
	v_mfma_f32_16x16x32_bf16 v[78:81], v[22:25], v[10:13], v[26:29]
	ds_read_b64_tr_b16 v[22:23], v182 offset:18560
	ds_read_b64_tr_b16 v[24:25], v182 offset:19712
	s_waitcnt lgkmcnt(0)
	v_mfma_f32_16x16x32_bf16 v[82:85], v[22:25], v[10:13], v[30:33]
	ds_read_b64_tr_b16 v[22:23], v182 offset:18592
	ds_read_b64_tr_b16 v[24:25], v182 offset:19744
	s_waitcnt lgkmcnt(0)
	v_mfma_f32_16x16x32_bf16 v[70:73], v[22:25], v[10:13], v[70:73]
	ds_read_b64_tr_b16 v[22:23], v182 offset:18624
	ds_read_b64_tr_b16 v[24:25], v182 offset:19776
	s_waitcnt lgkmcnt(0)
	v_mfma_f32_16x16x32_bf16 v[74:77], v[22:25], v[10:13], v[74:77]
	ds_read_b64_tr_b16 v[22:23], v182 offset:18656
	ds_read_b64_tr_b16 v[24:25], v182 offset:19808
	s_waitcnt lgkmcnt(0)
	v_mfma_f32_16x16x32_bf16 v[2:5], v[22:25], v[10:13], v[2:5]
	ds_read_b64_tr_b16 v[10:11], v182 offset:27648
	ds_read_b64_tr_b16 v[12:13], v182 offset:28800
	s_waitcnt vmcnt(8) lgkmcnt(0)
	v_mfma_f32_16x16x32_bf16 v[30:33], v[10:13], v[66:69], v[6:9]
	s_nop 2
	ds_read_b64_tr_b16 v[6:7], v182 offset:27680
	ds_read_b64_tr_b16 v[8:9], v182 offset:28832
	s_waitcnt lgkmcnt(0)
	v_mfma_f32_16x16x32_bf16 v[26:29], v[6:9], v[66:69], v[14:17]
	ds_read_b64_tr_b16 v[6:7], v182 offset:27712
	ds_read_b64_tr_b16 v[8:9], v182 offset:28864
	s_waitcnt lgkmcnt(0)
	v_mfma_f32_16x16x32_bf16 v[22:25], v[6:9], v[66:69], v[18:21]
	ds_read_b64_tr_b16 v[6:7], v182 offset:27744
	ds_read_b64_tr_b16 v[8:9], v182 offset:28896
	s_waitcnt lgkmcnt(0)
	v_mfma_f32_16x16x32_bf16 v[18:21], v[6:9], v[66:69], v[78:81]
	ds_read_b64_tr_b16 v[6:7], v182 offset:27776
	ds_read_b64_tr_b16 v[8:9], v182 offset:28928
	s_waitcnt lgkmcnt(0)
	v_mfma_f32_16x16x32_bf16 v[14:17], v[6:9], v[66:69], v[82:85]
	ds_read_b64_tr_b16 v[6:7], v182 offset:27808
	ds_read_b64_tr_b16 v[8:9], v182 offset:28960
	s_waitcnt lgkmcnt(0)
	v_mfma_f32_16x16x32_bf16 v[10:13], v[6:9], v[66:69], v[70:73]
	ds_read_b64_tr_b16 v[6:7], v182 offset:27840
	ds_read_b64_tr_b16 v[8:9], v182 offset:28992
	s_nop 0
	ds_read_b64_tr_b16 v[70:71], v182 offset:27872
	ds_read_b64_tr_b16 v[72:73], v182 offset:29024
	s_waitcnt lgkmcnt(0)
	s_waitcnt lgkmcnt(2)
	v_mfma_f32_16x16x32_bf16 v[6:9], v[6:9], v[66:69], v[74:77]
	s_barrier
; __device__ __forceinline__ float bflo(unsigned w) { return __uint_as_float(w << 16); }
; __device__ __forceinline__ float bfhi(unsigned w) { return __uint_as_float(w & 0xffff0000u); }
; __device__ __forceinline__ float gelu_fast(float x) { const float y = 1.5957691216057308f * (x + 0.044715f * x * x * x); return x * __builtin_amdgcn_rcpf(1.f + __expf(-y)); }
; __device__ __forceinline__ void gmlp_fast_unit(int ci, const bf16_t* P, const float* gnorm, const bf16_t* Wb, const float* bs_, bf16_t* AO, LAS unsigned char* lds) {
;     ...
;         const float bias = bsl[g * 128 + p];
;         bf16_t* op = AO + (size_t)(row0 + p) * D + 1024 + g * 128 + 4 * q;
; #pragma unroll
;         for (int ct = 0; ct < 8; ++ct) { const u32x2 uw = uwv[ct];
;             u32x2 o; o.x = pk2(gelu_fast(bflo(uw.x)) * (acc[ct][0] + bias), gelu_fast(bfhi(uw.x)) * (acc[ct][1] + bias));
;             o.y = pk2(gelu_fast(bflo(uw.y)) * (acc[ct][2] + bias), gelu_fast(bfhi(uw.y)) * (acc[ct][3] + bias));
;             *(u32x2*)(op + 16 * ct) = o; }
	ds_read_b32 v64, v64
	s_waitcnt lgkmcnt(1)
	v_mfma_f32_16x16x32_bf16 v[2:5], v[70:73], v[66:69], v[2:5]
	s_waitcnt vmcnt(7)
	v_lshlrev_b32_e32 v68, 16, v62
	v_and_b32_e32 v69, 0xffff0000, v62
	v_mul_f32_e32 v62, 0x3d372713, v68
	v_mul_f32_e32 v62, v62, v68
	v_mov_b32_e32 v70, v68
	v_fmac_f32_e32 v70, v62, v70
	v_mul_f32_e32 v62, 0xbfcc422a, v70
	v_mul_f32_e32 v62, 0x3fb8aa3b, v62
	v_exp_f32_e32 v62, v62
	v_mov_b32_e32 v71, v69
	s_waitcnt lgkmcnt(0)
	v_pk_add_f32 v[30:31], v[30:31], v[64:65] op_sel_hi:[1,0]
	v_pk_add_f32 v[32:33], v[32:33], v[64:65] op_sel_hi:[1,0]
	v_add_f32_e32 v62, 1.0, v62
	v_rcp_f32_e32 v70, v62
	v_mul_f32_e32 v62, 0x3d372713, v69
	v_mul_f32_e32 v62, v62, v69
	v_fmac_f32_e32 v71, v62, v71
	v_mul_f32_e32 v62, 0xbfcc422a, v71
	v_mul_f32_e32 v62, 0x3fb8aa3b, v62
	v_exp_f32_e32 v62, v62
	v_lshl_add_u64 v[66:67], s[94:95], 0, v[36:37]
	v_pk_add_f32 v[26:27], v[26:27], v[64:65] op_sel_hi:[1,0]
	v_pk_add_f32 v[28:29], v[28:29], v[64:65] op_sel_hi:[1,0]
	v_add_f32_e32 v62, 1.0, v62
	v_rcp_f32_e32 v71, v62
	v_pk_add_f32 v[22:23], v[22:23], v[64:65] op_sel_hi:[1,0]
	v_pk_add_f32 v[24:25], v[24:25], v[64:65] op_sel_hi:[1,0]
	v_pk_add_f32 v[18:19], v[18:19], v[64:65] op_sel_hi:[1,0]
	v_pk_mul_f32 v[68:69], v[70:71], v[68:69]
	v_pk_add_f32 v[20:21], v[20:21], v[64:65] op_sel_hi:[1,0]
	v_pk_mul_f32 v[30:31], v[68:69], v[30:31]
	v_pk_add_f32 v[14:15], v[14:15], v[64:65] op_sel_hi:[1,0]
	v_cvt_pk_bf16_f32 v62, v30, v31
	v_lshlrev_b32_e32 v30, 16, v63
	v_and_b32_e32 v31, 0xffff0000, v63
	v_mul_f32_e32 v63, 0x3d372713, v30
	v_mul_f32_e32 v63, v63, v30
	v_mov_b32_e32 v68, v30
	v_fmac_f32_e32 v68, v63, v68
	v_mul_f32_e32 v63, 0xbfcc422a, v68
	v_mul_f32_e32 v63, 0x3fb8aa3b, v63
	v_exp_f32_e32 v63, v63
	v_mov_b32_e32 v69, v31
	v_pk_add_f32 v[16:17], v[16:17], v[64:65] op_sel_hi:[1,0]
	v_pk_add_f32 v[10:11], v[10:11], v[64:65] op_sel_hi:[1,0]
	v_add_f32_e32 v63, 1.0, v63
	v_rcp_f32_e32 v68, v63
	v_mul_f32_e32 v63, 0x3d372713, v31
	v_mul_f32_e32 v63, v63, v31
	v_fmac_f32_e32 v69, v63, v69
	v_mul_f32_e32 v63, 0xbfcc422a, v69
	v_mul_f32_e32 v63, 0x3fb8aa3b, v63
	v_exp_f32_e32 v63, v63
	v_pk_add_f32 v[12:13], v[12:13], v[64:65] op_sel_hi:[1,0]
	v_pk_add_f32 v[6:7], v[6:7], v[64:65] op_sel_hi:[1,0]
	v_pk_add_f32 v[8:9], v[8:9], v[64:65] op_sel_hi:[1,0]
	v_add_f32_e32 v63, 1.0, v63
	v_rcp_f32_e32 v69, v63
	v_pk_add_f32 v[2:3], v[2:3], v[64:65] op_sel_hi:[1,0]
	v_pk_add_f32 v[4:5], v[4:5], v[64:65] op_sel_hi:[1,0]
	v_lshl_add_u64 v[36:37], v[36:37], 0, s[20:21]
	v_pk_mul_f32 v[30:31], v[68:69], v[30:31]
	s_nop 0
	v_pk_mul_f32 v[30:31], v[30:31], v[32:33]
	s_waitcnt vmcnt(6)
	v_lshlrev_b32_e32 v32, 16, v60
	v_cvt_pk_bf16_f32 v63, v30, v31
	v_add_co_u32_e32 v30, vcc, s3, v66
	v_and_b32_e32 v33, 0xffff0000, v60
	s_nop 0
	v_addc_co_u32_e32 v31, vcc, 0, v67, vcc
	v_mul_f32_e32 v60, 0x3d372713, v32
	global_store_dwordx2 v[30:31], v[62:63], off offset:2048
	v_mul_f32_e32 v60, v60, v32
	v_mov_b32_e32 v62, v32
	v_fmac_f32_e32 v62, v60, v62
	v_mul_f32_e32 v60, 0xbfcc422a, v62
	v_mul_f32_e32 v60, 0x3fb8aa3b, v60
	v_exp_f32_e32 v60, v60
	v_mov_b32_e32 v63, v33
	v_add_f32_e32 v60, 1.0, v60
	v_rcp_f32_e32 v62, v60
	v_mul_f32_e32 v60, 0x3d372713, v33
	v_mul_f32_e32 v60, v60, v33
	v_fmac_f32_e32 v63, v60, v63
	v_mul_f32_e32 v60, 0xbfcc422a, v63
	v_mul_f32_e32 v60, 0x3fb8aa3b, v60
	v_exp_f32_e32 v60, v60
	s_nop 0
	v_add_f32_e32 v60, 1.0, v60
	v_rcp_f32_e32 v63, v60
	s_nop 0
	v_pk_mul_f32 v[32:33], v[62:63], v[32:33]
	s_nop 0
	v_pk_mul_f32 v[26:27], v[32:33], v[26:27]
	v_lshlrev_b32_e32 v32, 16, v61
	v_cvt_pk_bf16_f32 v26, v26, v27
	v_mul_f32_e32 v27, 0x3d372713, v32
	v_mul_f32_e32 v27, v27, v32
	v_mov_b32_e32 v60, v32
	v_fmac_f32_e32 v60, v27, v60
	v_mul_f32_e32 v27, 0xbfcc422a, v60
	v_mul_f32_e32 v27, 0x3fb8aa3b, v27
	v_exp_f32_e32 v27, v27
	v_and_b32_e32 v33, 0xffff0000, v61
	v_mov_b32_e32 v61, v33
	v_add_f32_e32 v27, 1.0, v27
	v_rcp_f32_e32 v60, v27
	v_mul_f32_e32 v27, 0x3d372713, v33
	v_mul_f32_e32 v27, v27, v33
	v_fmac_f32_e32 v61, v27, v61
	v_mul_f32_e32 v27, 0xbfcc422a, v61
	v_mul_f32_e32 v27, 0x3fb8aa3b, v27
	v_exp_f32_e32 v27, v27
	s_nop 0
	v_add_f32_e32 v27, 1.0, v27
	v_rcp_f32_e32 v61, v27
	s_nop 0
	v_pk_mul_f32 v[32:33], v[60:61], v[32:33]
	s_nop 0
	v_pk_mul_f32 v[28:29], v[32:33], v[28:29]
	s_nop 0
	v_cvt_pk_bf16_f32 v27, v28, v29
	global_store_dwordx2 v[30:31], v[26:27], off offset:2080
	s_waitcnt vmcnt(7)
	v_lshlrev_b32_e32 v26, 16, v58
	v_mul_f32_e32 v28, 0x3d372713, v26
	v_mul_f32_e32 v28, v28, v26
	v_mov_b32_e32 v29, v26
	v_and_b32_e32 v27, 0xffff0000, v58
	v_fmac_f32_e32 v29, v28, v29
	v_mul_f32_e32 v28, 0xbfcc422a, v29
	v_mul_f32_e32 v29, 0x3d372713, v27
	v_mul_f32_e32 v29, v29, v27
	v_mov_b32_e32 v32, v27
	v_fmac_f32_e32 v32, v29, v32
	v_mul_f32_e32 v29, 0xbfcc422a, v32
	v_mul_f32_e32 v28, 0x3fb8aa3b, v28
	v_mul_f32_e32 v29, 0x3fb8aa3b, v29
	v_exp_f32_e32 v28, v28
	v_exp_f32_e32 v29, v29
	v_add_f32_e32 v28, 1.0, v28
	v_add_f32_e32 v29, 1.0, v29
	v_rcp_f32_e32 v28, v28
	v_rcp_f32_e32 v29, v29
	s_nop 0
	v_pk_mul_f32 v[26:27], v[28:29], v[26:27]
	s_nop 0
	v_pk_mul_f32 v[22:23], v[26:27], v[22:23]
	v_lshlrev_b32_e32 v26, 16, v59
	v_cvt_pk_bf16_f32 v22, v22, v23
	v_mul_f32_e32 v23, 0x3d372713, v26
	v_mul_f32_e32 v23, v23, v26
	v_mov_b32_e32 v28, v26
	v_fmac_f32_e32 v28, v23, v28
	v_mul_f32_e32 v23, 0xbfcc422a, v28
	v_mul_f32_e32 v23, 0x3fb8aa3b, v23
	v_exp_f32_e32 v23, v23
	v_and_b32_e32 v27, 0xffff0000, v59
	v_mov_b32_e32 v29, v27
	v_add_f32_e32 v23, 1.0, v23
	v_rcp_f32_e32 v28, v23
	v_mul_f32_e32 v23, 0x3d372713, v27
	v_mul_f32_e32 v23, v23, v27
	v_fmac_f32_e32 v29, v23, v29
	v_mul_f32_e32 v23, 0xbfcc422a, v29
	v_mul_f32_e32 v23, 0x3fb8aa3b, v23
	v_exp_f32_e32 v23, v23
	s_nop 0
	v_add_f32_e32 v23, 1.0, v23
	v_rcp_f32_e32 v29, v23
	s_nop 0
	v_pk_mul_f32 v[26:27], v[28:29], v[26:27]
	s_nop 0
	v_pk_mul_f32 v[24:25], v[26:27], v[24:25]
	s_nop 0
	v_cvt_pk_bf16_f32 v23, v24, v25
	global_store_dwordx2 v[30:31], v[22:23], off offset:2112
	s_waitcnt vmcnt(7)
; __device__ __forceinline__ float bflo(unsigned w) { return __uint_as_float(w << 16); }
; __device__ __forceinline__ float bfhi(unsigned w) { return __uint_as_float(w & 0xffff0000u); }
; __device__ __forceinline__ float gelu_fast(float x) { const float y = 1.5957691216057308f * (x + 0.044715f * x * x * x); return x * __builtin_amdgcn_rcpf(1.f + __expf(-y)); }
; __device__ __forceinline__ void gmlp_fast_unit(int ci, const bf16_t* P, const float* gnorm, const bf16_t* Wb, const float* bs_, bf16_t* AO, LAS unsigned char* lds) {
;     ...
;         const float bias = bsl[g * 128 + p];
;         bf16_t* op = AO + (size_t)(row0 + p) * D + 1024 + g * 128 + 4 * q;
; #pragma unroll
;         for (int ct = 0; ct < 8; ++ct) { const u32x2 uw = uwv[ct];
;             u32x2 o; o.x = pk2(gelu_fast(bflo(uw.x)) * (acc[ct][0] + bias), gelu_fast(bfhi(uw.x)) * (acc[ct][1] + bias));
;             o.y = pk2(gelu_fast(bflo(uw.y)) * (acc[ct][2] + bias), gelu_fast(bfhi(uw.y)) * (acc[ct][3] + bias));
;             *(u32x2*)(op + 16 * ct) = o; }
	v_lshlrev_b32_e32 v22, 16, v56
	v_mul_f32_e32 v24, 0x3d372713, v22
	v_mul_f32_e32 v24, v24, v22
	v_mov_b32_e32 v25, v22
	v_and_b32_e32 v23, 0xffff0000, v56
	v_fmac_f32_e32 v25, v24, v25
	v_mul_f32_e32 v24, 0xbfcc422a, v25
	v_mul_f32_e32 v25, 0x3d372713, v23
	v_mul_f32_e32 v25, v25, v23
	v_mov_b32_e32 v26, v23
	v_fmac_f32_e32 v26, v25, v26
	v_mul_f32_e32 v25, 0xbfcc422a, v26
	v_mul_f32_e32 v24, 0x3fb8aa3b, v24
	v_mul_f32_e32 v25, 0x3fb8aa3b, v25
	v_exp_f32_e32 v24, v24
	v_exp_f32_e32 v25, v25
	v_add_f32_e32 v24, 1.0, v24
	v_add_f32_e32 v25, 1.0, v25
	v_rcp_f32_e32 v24, v24
	v_rcp_f32_e32 v25, v25
	s_nop 0
	v_pk_mul_f32 v[22:23], v[24:25], v[22:23]
	s_nop 0
	v_pk_mul_f32 v[18:19], v[22:23], v[18:19]
	v_lshlrev_b32_e32 v22, 16, v57
	v_cvt_pk_bf16_f32 v18, v18, v19
	v_mul_f32_e32 v19, 0x3d372713, v22
	v_mul_f32_e32 v19, v19, v22
	v_mov_b32_e32 v24, v22
	v_fmac_f32_e32 v24, v19, v24
	v_mul_f32_e32 v19, 0xbfcc422a, v24
	v_mul_f32_e32 v19, 0x3fb8aa3b, v19
	v_exp_f32_e32 v19, v19
	v_and_b32_e32 v23, 0xffff0000, v57
	v_mov_b32_e32 v25, v23
	v_add_f32_e32 v19, 1.0, v19
	v_rcp_f32_e32 v24, v19
	v_mul_f32_e32 v19, 0x3d372713, v23
	v_mul_f32_e32 v19, v19, v23
	v_fmac_f32_e32 v25, v19, v25
	v_mul_f32_e32 v19, 0xbfcc422a, v25
	v_mul_f32_e32 v19, 0x3fb8aa3b, v19
	v_exp_f32_e32 v19, v19
	s_nop 0
	v_add_f32_e32 v19, 1.0, v19
	v_rcp_f32_e32 v25, v19
	s_nop 0
	v_pk_mul_f32 v[22:23], v[24:25], v[22:23]
	s_nop 0
	v_pk_mul_f32 v[20:21], v[22:23], v[20:21]
	s_nop 0
	v_cvt_pk_bf16_f32 v19, v20, v21
	global_store_dwordx2 v[30:31], v[18:19], off offset:2144
	s_waitcnt vmcnt(7)
	v_lshlrev_b32_e32 v18, 16, v54
	v_mul_f32_e32 v20, 0x3d372713, v18
	v_mul_f32_e32 v20, v20, v18
	v_mov_b32_e32 v21, v18
	v_and_b32_e32 v19, 0xffff0000, v54
	v_fmac_f32_e32 v21, v20, v21
	v_mul_f32_e32 v20, 0xbfcc422a, v21
	v_mul_f32_e32 v21, 0x3d372713, v19
	v_mul_f32_e32 v21, v21, v19
	v_mov_b32_e32 v22, v19
	v_fmac_f32_e32 v22, v21, v22
	v_mul_f32_e32 v21, 0xbfcc422a, v22
	v_mul_f32_e32 v20, 0x3fb8aa3b, v20
	v_mul_f32_e32 v21, 0x3fb8aa3b, v21
	v_exp_f32_e32 v20, v20
	v_exp_f32_e32 v21, v21
	v_add_f32_e32 v20, 1.0, v20
	v_add_f32_e32 v21, 1.0, v21
	v_rcp_f32_e32 v20, v20
	v_rcp_f32_e32 v21, v21
	s_nop 0
	v_pk_mul_f32 v[18:19], v[20:21], v[18:19]
	s_nop 0
	v_pk_mul_f32 v[14:15], v[18:19], v[14:15]
	v_lshlrev_b32_e32 v18, 16, v55
	v_cvt_pk_bf16_f32 v14, v14, v15
	v_mul_f32_e32 v15, 0x3d372713, v18
	v_mul_f32_e32 v15, v15, v18
	v_mov_b32_e32 v20, v18
	v_fmac_f32_e32 v20, v15, v20
	v_mul_f32_e32 v15, 0xbfcc422a, v20
	v_mul_f32_e32 v15, 0x3fb8aa3b, v15
	v_exp_f32_e32 v15, v15
	v_and_b32_e32 v19, 0xffff0000, v55
	v_mov_b32_e32 v21, v19
	v_add_f32_e32 v15, 1.0, v15
	v_rcp_f32_e32 v20, v15
	v_mul_f32_e32 v15, 0x3d372713, v19
	v_mul_f32_e32 v15, v15, v19
	v_fmac_f32_e32 v21, v15, v21
	v_mul_f32_e32 v15, 0xbfcc422a, v21
	v_mul_f32_e32 v15, 0x3fb8aa3b, v15
	v_exp_f32_e32 v15, v15
	s_nop 0
	v_add_f32_e32 v15, 1.0, v15
	v_rcp_f32_e32 v21, v15
	s_nop 0
	v_pk_mul_f32 v[18:19], v[20:21], v[18:19]
	s_nop 0
	v_pk_mul_f32 v[16:17], v[18:19], v[16:17]
	s_nop 0
	v_cvt_pk_bf16_f32 v15, v16, v17
	global_store_dwordx2 v[30:31], v[14:15], off offset:2176
	s_waitcnt vmcnt(7)
; __device__ __forceinline__ float bflo(unsigned w) { return __uint_as_float(w << 16); }
; __device__ __forceinline__ float bfhi(unsigned w) { return __uint_as_float(w & 0xffff0000u); }
; __device__ __forceinline__ float gelu_fast(float x) { const float y = 1.5957691216057308f * (x + 0.044715f * x * x * x); return x * __builtin_amdgcn_rcpf(1.f + __expf(-y)); }
; __device__ __forceinline__ void gmlp_fast_unit(int ci, const bf16_t* P, const float* gnorm, const bf16_t* Wb, const float* bs_, bf16_t* AO, LAS unsigned char* lds) {
;     ...
;         const float bias = bsl[g * 128 + p];
;         bf16_t* op = AO + (size_t)(row0 + p) * D + 1024 + g * 128 + 4 * q;
; #pragma unroll
;         for (int ct = 0; ct < 8; ++ct) { const u32x2 uw = uwv[ct];
;             u32x2 o; o.x = pk2(gelu_fast(bflo(uw.x)) * (acc[ct][0] + bias), gelu_fast(bfhi(uw.x)) * (acc[ct][1] + bias));
;             o.y = pk2(gelu_fast(bflo(uw.y)) * (acc[ct][2] + bias), gelu_fast(bfhi(uw.y)) * (acc[ct][3] + bias));
;             *(u32x2*)(op + 16 * ct) = o; }
;     }
	v_lshlrev_b32_e32 v14, 16, v52
	v_mul_f32_e32 v16, 0x3d372713, v14
	v_mul_f32_e32 v16, v16, v14
	v_mov_b32_e32 v17, v14
	v_and_b32_e32 v15, 0xffff0000, v52
	v_fmac_f32_e32 v17, v16, v17
	v_mul_f32_e32 v16, 0xbfcc422a, v17
	v_mul_f32_e32 v17, 0x3d372713, v15
	v_mul_f32_e32 v17, v17, v15
	v_mov_b32_e32 v18, v15
	v_fmac_f32_e32 v18, v17, v18
	v_mul_f32_e32 v17, 0xbfcc422a, v18
	v_mul_f32_e32 v16, 0x3fb8aa3b, v16
	v_mul_f32_e32 v17, 0x3fb8aa3b, v17
	v_exp_f32_e32 v16, v16
	v_exp_f32_e32 v17, v17
	v_add_f32_e32 v16, 1.0, v16
	v_add_f32_e32 v17, 1.0, v17
	v_rcp_f32_e32 v16, v16
	v_rcp_f32_e32 v17, v17
	s_nop 0
	v_pk_mul_f32 v[14:15], v[16:17], v[14:15]
	s_nop 0
	v_pk_mul_f32 v[10:11], v[14:15], v[10:11]
	v_lshlrev_b32_e32 v14, 16, v53
	v_cvt_pk_bf16_f32 v10, v10, v11
	v_mul_f32_e32 v11, 0x3d372713, v14
	v_mul_f32_e32 v11, v11, v14
	v_mov_b32_e32 v16, v14
	v_fmac_f32_e32 v16, v11, v16
	v_mul_f32_e32 v11, 0xbfcc422a, v16
	v_mul_f32_e32 v11, 0x3fb8aa3b, v11
	v_exp_f32_e32 v11, v11
	v_and_b32_e32 v15, 0xffff0000, v53
	v_mov_b32_e32 v17, v15
	v_add_f32_e32 v11, 1.0, v11
	v_rcp_f32_e32 v16, v11
	v_mul_f32_e32 v11, 0x3d372713, v15
	v_mul_f32_e32 v11, v11, v15
	v_fmac_f32_e32 v17, v11, v17
	v_mul_f32_e32 v11, 0xbfcc422a, v17
	v_mul_f32_e32 v11, 0x3fb8aa3b, v11
	v_exp_f32_e32 v11, v11
	s_nop 0
	v_add_f32_e32 v11, 1.0, v11
	v_rcp_f32_e32 v17, v11
	s_nop 0
	v_pk_mul_f32 v[14:15], v[16:17], v[14:15]
	s_nop 0
	v_pk_mul_f32 v[12:13], v[14:15], v[12:13]
	s_nop 0
	v_cvt_pk_bf16_f32 v11, v12, v13
	global_store_dwordx2 v[30:31], v[10:11], off offset:2208
	s_waitcnt vmcnt(7)
	v_lshlrev_b32_e32 v10, 16, v50
	v_mul_f32_e32 v12, 0x3d372713, v10
	v_mul_f32_e32 v12, v12, v10
	v_mov_b32_e32 v13, v10
	v_and_b32_e32 v11, 0xffff0000, v50
	v_fmac_f32_e32 v13, v12, v13
	v_mul_f32_e32 v12, 0xbfcc422a, v13
	v_mul_f32_e32 v13, 0x3d372713, v11
	v_mul_f32_e32 v13, v13, v11
	v_mov_b32_e32 v14, v11
	v_fmac_f32_e32 v14, v13, v14
	v_mul_f32_e32 v13, 0xbfcc422a, v14
	v_mul_f32_e32 v12, 0x3fb8aa3b, v12
	v_mul_f32_e32 v13, 0x3fb8aa3b, v13
	v_exp_f32_e32 v12, v12
	v_exp_f32_e32 v13, v13
	v_add_f32_e32 v12, 1.0, v12
	v_add_f32_e32 v13, 1.0, v13
	v_rcp_f32_e32 v12, v12
	v_rcp_f32_e32 v13, v13
	s_nop 0
	v_pk_mul_f32 v[10:11], v[12:13], v[10:11]
	s_nop 0
	v_pk_mul_f32 v[6:7], v[10:11], v[6:7]
	v_lshlrev_b32_e32 v10, 16, v51
	v_cvt_pk_bf16_f32 v6, v6, v7
	v_mul_f32_e32 v7, 0x3d372713, v10
	v_mul_f32_e32 v7, v7, v10
	v_mov_b32_e32 v12, v10
	v_fmac_f32_e32 v12, v7, v12
	v_mul_f32_e32 v7, 0xbfcc422a, v12
	v_mul_f32_e32 v7, 0x3fb8aa3b, v7
	v_exp_f32_e32 v7, v7
	v_and_b32_e32 v11, 0xffff0000, v51
	v_mov_b32_e32 v13, v11
	v_add_f32_e32 v7, 1.0, v7
	v_rcp_f32_e32 v12, v7
	v_mul_f32_e32 v7, 0x3d372713, v11
	v_mul_f32_e32 v7, v7, v11
	v_fmac_f32_e32 v13, v7, v13
	v_mul_f32_e32 v7, 0xbfcc422a, v13
	v_mul_f32_e32 v7, 0x3fb8aa3b, v7
	v_exp_f32_e32 v7, v7
	s_nop 0
	v_add_f32_e32 v7, 1.0, v7
	v_rcp_f32_e32 v13, v7
	s_nop 0
	v_pk_mul_f32 v[10:11], v[12:13], v[10:11]
	s_nop 0
	v_pk_mul_f32 v[8:9], v[10:11], v[8:9]
	s_nop 0
	v_cvt_pk_bf16_f32 v7, v8, v9
	global_store_dwordx2 v[30:31], v[6:7], off offset:2240
	s_waitcnt vmcnt(7)
	v_lshlrev_b32_e32 v6, 16, v48
	v_mul_f32_e32 v8, 0x3d372713, v6
	v_mul_f32_e32 v8, v8, v6
	v_mov_b32_e32 v9, v6
	v_and_b32_e32 v7, 0xffff0000, v48
	v_fmac_f32_e32 v9, v8, v9
	v_mul_f32_e32 v8, 0xbfcc422a, v9
	v_mul_f32_e32 v9, 0x3d372713, v7
	v_mul_f32_e32 v9, v9, v7
	v_mov_b32_e32 v10, v7
	v_fmac_f32_e32 v10, v9, v10
	v_mul_f32_e32 v9, 0xbfcc422a, v10
	v_mul_f32_e32 v8, 0x3fb8aa3b, v8
	v_mul_f32_e32 v9, 0x3fb8aa3b, v9
	v_exp_f32_e32 v8, v8
	v_exp_f32_e32 v9, v9
	v_add_f32_e32 v8, 1.0, v8
	v_add_f32_e32 v9, 1.0, v9
	v_rcp_f32_e32 v8, v8
	v_rcp_f32_e32 v9, v9
	s_nop 0
	v_pk_mul_f32 v[6:7], v[8:9], v[6:7]
	s_nop 0
	v_pk_mul_f32 v[2:3], v[6:7], v[2:3]
	v_lshlrev_b32_e32 v6, 16, v49
	v_cvt_pk_bf16_f32 v2, v2, v3
	v_mul_f32_e32 v3, 0x3d372713, v6
	v_mul_f32_e32 v3, v3, v6
	v_mov_b32_e32 v8, v6
	v_fmac_f32_e32 v8, v3, v8
	v_mul_f32_e32 v3, 0xbfcc422a, v8
	v_mul_f32_e32 v3, 0x3fb8aa3b, v3
	v_exp_f32_e32 v3, v3
	v_and_b32_e32 v7, 0xffff0000, v49
	v_mov_b32_e32 v9, v7
	v_add_f32_e32 v3, 1.0, v3
	v_rcp_f32_e32 v8, v3
	v_mul_f32_e32 v3, 0x3d372713, v7
	v_mul_f32_e32 v3, v3, v7
	v_fmac_f32_e32 v9, v3, v9
	v_mul_f32_e32 v3, 0xbfcc422a, v9
	v_mul_f32_e32 v3, 0x3fb8aa3b, v3
	v_exp_f32_e32 v3, v3
	s_nop 0
	v_add_f32_e32 v3, 1.0, v3
	v_rcp_f32_e32 v9, v3
	s_nop 0
	v_pk_mul_f32 v[6:7], v[8:9], v[6:7]
	s_nop 0
	v_pk_mul_f32 v[4:5], v[6:7], v[4:5]
	s_nop 0
	v_cvt_pk_bf16_f32 v3, v4, v5
	global_store_dwordx2 v[30:31], v[2:3], off offset:2272
	s_cbranch_scc0 .LBB0_293
	s_branch .LBB0_274
